# moe1 gather GEMM: next-unit perm row load issued one K-loop trip earlier (into constant VGPRs that are restored), removing the in-loop vmcnt(0) drain
# speedup vs baseline: 1.0187x; 1.0001x over previous
.LBB0_2372:
	s_cmpk_eq_i32 s22, 0x600
	s_cselect_b64 s[4:5], -1, 0
	s_and_b64 s[26:27], s[0:1], s[4:5]
	s_andn2_b64 vcc, exec, s[26:27]
	s_cbranch_vccnz .Lmy_ar_m1_skip
	s_movk_i32 s26, 0x100
	v_cmp_gt_i32_e32 vcc, s26, v0
	s_and_saveexec_b64 s[26:27], vcc
	s_cbranch_execz .Lmy_ar_m1_rest
	v_add_u32_e32 v132, v0, v237
	v_cmp_lt_i32_e32 vcc, v132, v238
	s_nop 1
	v_cndmask_b32_e32 v132, v237, v132, vcc
	v_ashrrev_i32_e32 v133, 31, v132
	v_lshl_add_u64 v[132:133], v[132:133], 4, v[200:201]
	global_load_dwordx2 v[226:227], v[132:133], off
	global_load_dword v228, v[132:133], off offset:8
	global_load_dword v219, v[132:133], off offset:12

.Lmy_ar_m1_skip:
	s_cmpk_eq_i32 s22, 0x700
	s_cselect_b64 s[4:5], -1, 0
	s_and_b64 s[26:27], s[0:1], s[4:5]
	v_cndmask_b32_e64 v2, 0, 1, s[26:27]
	v_cmp_ne_u32_e64 s[8:9], 1, v2
	s_andn2_b64 vcc, exec, s[26:27]
	s_cbranch_vccnz .LBB0_2376
	v_mov_b32_e32 v2, v0
	s_movk_i32 s26, 0x100
	s_nop 0
	v_cmp_gt_i32_e32 vcc, s26, v2
	s_and_saveexec_b64 s[26:27], vcc
	s_cbranch_execz .LBB0_2375
	v_add_u32_e32 v132, v2, v237
	v_cmp_lt_i32_e32 vcc, v132, v238
	v_add_u32_e32 v2, s44, v2
	v_lshl_add_u32 v2, v2, 2, 0
	v_cndmask_b32_e32 v132, v237, v132, vcc
	v_ashrrev_i32_e32 v133, 31, v132
	v_add_u32_e32 v136, 0x20100, v2
	v_mov_b32_e32 v132, v226
	v_mov_b32_e32 v133, v227
	v_mov_b32_e32 v134, v228
	v_mov_b32_e32 v135, v219
	v_mov_b32_e32 v226, 0x180
	v_mov_b32_e32 v227, 0x2080
	v_mov_b32_e32 v228, 0xff61b1e6
	v_mov_b32_e32 v219, 0x3b808081
	v_cndmask_b32_e32 v132, -1, v132, vcc
	ds_write_b32 v136, v132
	v_add_u32_e32 v132, 0x20900, v2
	ds_write_b32 v132, v133
	v_cndmask_b32_e64 v132, v135, v134, s[2:3]
	v_add_u32_e32 v2, 0x21100, v2
	ds_write_b32 v2, v132
